# MLA: stage barrier moved behind the odd tile's QK MFMAs; the even tile's first K fragments are prefetched from LDS in the odd tile's PV/exp gaps
# baseline (speedup 1.0000x reference)
; #define LAS __attribute__((address_space(3)))
; #define WAITV(n) asm volatile("s_waitcnt vmcnt(%0)" ::"n"(n) : "memory")
; #define SBAR() do { asm volatile("s_waitcnt lgkmcnt(0)" ::: "memory"); __builtin_amdgcn_s_barrier(); asm volatile("" ::: "memory"); } while (0)
; DEV float ex2(float x) { return __builtin_amdgcn_exp2f(x); }
; #define MLA_SB() __builtin_amdgcn_sched_barrier(0)
; #define MLA_PIN(x) asm volatile("" : "+v"(x))
; template <int VAR> DEV void mla_step(f32x16& C0, f32x16& C1, f32x16& P0, f32x16& P1, f32x16& o0, f32x16& o1, f32x16& lacc,
;                   const v8i (&qf)[2], const f32x16& cini, LAS char* kp, LAS char* vp, v8i& pw) {
;     v8i kf[2], vf[2];
;     const v8i ones8 = {0x38383838, 0x38383838, 0x38383838, 0x38383838, 0x38383838, 0x38383838, 0x38383838, 0x38383838};
;     kf[0] = mla_kf8(kp, 0, 0); kf[1] = mla_kf8(kp, 1, 0);
;     MLA_SB();
; #pragma unroll
;     for (int g = 0; g < 4; ++g) {
;         const int kb = g & 1, sx = g >> 1;
;         if (kb) C1 = MFMA8(kf[1], qf[sx], sx == 0 ? cini : C1); else C0 = MFMA8(kf[0], qf[sx], sx == 0 ? cini : C0);
;         if (g < 2) kf[kb] = mla_kf8(kp, kb, 1);
;         if (g >= 2) vf[g - 2] = mla_vf8(vp, g - 2);
; #pragma unroll
;         for (int j = 0; j < 2; ++j) { const int w = 2 * g + j, e = 4 * w;
;             if (VAR == 3) pw[w] = __builtin_bit_cast(int, (e < 16) ? P0[e] : P1[e - 16]);
;             else pw[w] = (int)((e < 16) ? pk_bf8x4(P0[e], P0[e + 1], P0[e + 2], P0[e + 3], pw[w]) : pk_bf8x4(P1[e - 16], P1[e - 15], P1[e - 14], P1[e - 13], pw[w])); }
;         if (g == 3) MLA_PIN(pw);
;         MLA_SB();
;     }
; #pragma unroll
;     for (int g = 0; g < 3; ++g) {
;         if (g == 0) o0 = MFMA8PV(vf[0], pw, o0); else if (g == 1) o1 = MFMA8PV(vf[1], pw, o1); else lacc = MFMA8PV(ones8, pw, lacc);
;         const int e0 = (g * 32) / 3, e1 = ((g + 1) * 32) / 3;
; #pragma unroll
;         for (int e = e0; e < e1; ++e) { if (VAR == 2 || VAR == 3) continue; if (e < 16) C0[e] = ex2(C0[e]); else C1[e - 16] = ex2(C1[e - 16]); }
;         if (g < 2) MLA_PIN(C0);
;         if (g > 0) MLA_PIN(C1);
;         MLA_SB();
;     }
; }
; template <int VAR> DEV void mla_unit(const Params& p, int layer, int b, int hd, int tokbase, int t0, int t1, LAS char* lds, SideJob& sj) {
;     ...
;         if (s + 1 < ns) {
;             const int nslot = (slot == 2) ? 0 : slot + 1;
;             WAITV(0); SBAR();
.LBB0_812:
	s_mul_i32 s2, s62, 0x6000
	v_add_u32_e32 v172, s2, v200
	ds_read_b128 v[98:101], v172 offset:8192
	ds_read_b128 v[106:109], v172 offset:8704
	ds_read_b128 v[102:105], v172 offset:9216
	ds_read_b128 v[110:113], v172 offset:9728
	v_cvt_pk_bf8_f32 v146, v82, v83
	v_cvt_pk_bf8_f32 v147, v86, v87
	v_exp_f32_e32 v69, v69
	v_exp_f32_e32 v70, v70
	v_exp_f32_e32 v71, v71
	s_waitcnt lgkmcnt(1)
	v_mfma_scale_f32_32x32x64_f8f6f4 v[114:129], v[98:105], v[138:145], v[2:17], v209, v208 op_sel_hi:[0,0,0]
	ds_read_b128 v[154:157], v172 offset:12288
	ds_read_b128 v[158:161], v172 offset:13312
	v_cvt_pk_bf8_f32 v146, v84, v85 op_sel:[0,0,1]
	v_cvt_pk_bf8_f32 v147, v88, v89 op_sel:[0,0,1]
	v_cvt_pk_bf8_f32 v148, v90, v91
	v_cvt_pk_bf8_f32 v149, v94, v95
	ds_read_b128 v[82:85], v172 offset:12800
	ds_read_b128 v[86:89], v172 offset:13824
	v_exp_f32_e32 v72, v72
	v_exp_f32_e32 v73, v73
	s_waitcnt lgkmcnt(4)
	v_mfma_scale_f32_32x32x64_f8f6f4 v[98:113], v[106:113], v[138:145], v[2:17], v209, v208 op_sel_hi:[0,0,0]
	v_cvt_pk_bf8_f32 v148, v92, v93 op_sel:[0,0,1]
	v_cvt_pk_bf8_f32 v149, v96, v97 op_sel:[0,0,1]
	ds_read_b128 v[90:93], v172 offset:16384
	ds_read_b128 v[94:97], v172 offset:17408
	v_exp_f32_e32 v74, v74
	v_exp_f32_e32 v75, v75
	v_exp_f32_e32 v76, v76
	s_waitcnt lgkmcnt(4)
	v_mfma_scale_f32_32x32x64_f8f6f4 v[114:129], v[154:161], v[130:137], v[114:129], v209, v208 op_sel_hi:[0,0,0]
	v_exp_f32_e32 v77, v77
	v_exp_f32_e32 v78, v78
	v_exp_f32_e32 v79, v79
	v_exp_f32_e32 v80, v80
	v_exp_f32_e32 v81, v81
	s_waitcnt lgkmcnt(2)
	v_mfma_scale_f32_32x32x64_f8f6f4 v[98:113], v[82:89], v[130:137], v[98:113], v209, v208 op_sel_hi:[0,0,0]
	s_add_i32 s61, s61, 1
	s_add_i32 s2, s62, 1
	s_cmp_lg_u32 s62, 2
	s_cselect_b32 s62, s2, 0
	s_mul_i32 s64, s62, 0x6000
	s_add_i32 s2, s64, 0x6000
	s_cmp_eq_u32 s62, 2
	s_cselect_b64 s[8:9], -1, 0
	s_cmp_eq_u32 s100, 0
	s_cbranch_scc1 .Lmla_w0
	s_cmp_eq_u32 s100, 1
	s_cbranch_scc1 .Lmla_w1
	s_waitcnt vmcnt(2)
	s_branch .Lmla_wd

; #define LAS __attribute__((address_space(3)))
; #define WAITV(n) asm volatile("s_waitcnt vmcnt(%0)" ::"n"(n) : "memory")
; DEV float ex2(float x) { return __builtin_amdgcn_exp2f(x); }
; #define MLA_SB() __builtin_amdgcn_sched_barrier(0)
; template <int VAR> DEV void mla_step(f32x16& C0, f32x16& C1, f32x16& P0, f32x16& P1, f32x16& o0, f32x16& o1, f32x16& lacc,
;                   const v8i (&qf)[2], const f32x16& cini, LAS char* kp, LAS char* vp, v8i& pw) {
;     v8i kf[2], vf[2];
;     const v8i ones8 = {0x38383838, 0x38383838, 0x38383838, 0x38383838, 0x38383838, 0x38383838, 0x38383838, 0x38383838};
;     kf[0] = mla_kf8(kp, 0, 0); kf[1] = mla_kf8(kp, 1, 0);
;     MLA_SB();
; #pragma unroll
;     for (int g = 0; g < 4; ++g) {
;         const int kb = g & 1, sx = g >> 1;
;         if (kb) C1 = MFMA8(kf[1], qf[sx], sx == 0 ? cini : C1); else C0 = MFMA8(kf[0], qf[sx], sx == 0 ? cini : C0);
;         if (g < 2) kf[kb] = mla_kf8(kp, kb, 1);
;         if (g >= 2) vf[g - 2] = mla_vf8(vp, g - 2);
; #pragma unroll
;         for (int j = 0; j < 2; ++j) { const int w = 2 * g + j, e = 4 * w;
;             if (VAR == 3) pw[w] = __builtin_bit_cast(int, (e < 16) ? P0[e] : P1[e - 16]);
;             else pw[w] = (int)((e < 16) ? pk_bf8x4(P0[e], P0[e + 1], P0[e + 2], P0[e + 3], pw[w]) : pk_bf8x4(P1[e - 16], P1[e - 15], P1[e - 14], P1[e - 13], pw[w])); }
;         if (g == 3) MLA_PIN(pw);
;         MLA_SB();
;     }
; #pragma unroll
;     for (int g = 0; g < 3; ++g) {
;         if (g == 0) o0 = MFMA8PV(vf[0], pw, o0); else if (g == 1) o1 = MFMA8PV(vf[1], pw, o1); else lacc = MFMA8PV(ones8, pw, lacc);
;         const int e0 = (g * 32) / 3, e1 = ((g + 1) * 32) / 3;
; #pragma unroll
;         for (int e = e0; e < e1; ++e) { if (VAR == 2 || VAR == 3) continue; if (e < 16) C0[e] = ex2(C0[e]); else C1[e - 16] = ex2(C1[e - 16]); }
;         if (g < 2) MLA_PIN(C0);
;         if (g > 0) MLA_PIN(C1);
;         MLA_SB();
;     }
; }
; template <int VAR> DEV void mla_unit(const Params& p, int layer, int b, int hd, int tokbase, int t0, int t1, LAS char* lds, SideJob& sj) {
;     ...
;             WAITV(0); SBAR();
;             if (s + 2 < ns) MLA_ISSUE(t0 + s + 2, (nslot == 2) ? 0 : nslot + 1);
;             { LAS char* nb = lds + nslot * STG; LAS char* ob = lds + slot * STG; mla_step<VAR>(sA0, sA1, sB0, sB1, o0, o1, lacc, qf, cini, nb + koffl, ob + MLA_VSUB + voffl, pw); }
.Lmla_wd:
	s_and_b64 s[20:21], s[8:9], exec
	s_waitcnt lgkmcnt(0)
	s_barrier
	s_cselect_b32 s2, 0, s2
	s_add_i32 s2, s2, s60
	s_mov_b32 s3, m0
	s_mov_b32 m0, s2
	v_cvt_pk_bf8_f32 v150, v66, v67
	v_cvt_pk_bf8_f32 v151, v70, v71
	v_cvt_pk_bf8_f32 v150, v68, v69 op_sel:[0,0,1]
	v_cvt_pk_bf8_f32 v151, v72, v73 op_sel:[0,0,1]
	v_cvt_pk_bf8_f32 v152, v74, v75
	v_cvt_pk_bf8_f32 v153, v78, v79
	v_cvt_pk_bf8_f32 v152, v76, v77 op_sel:[0,0,1]
	v_cvt_pk_bf8_f32 v153, v80, v81 op_sel:[0,0,1]
	ds_read_b128 v[66:69], v172 offset:16896
	ds_read_b128 v[70:73], v172 offset:17920
	s_waitcnt lgkmcnt(2)
	v_mfma_scale_f32_32x32x64_f8f6f4 v[50:65], v[90:97], v[146:153], v[50:65], v209, v209 op_sel_hi:[0,0,0] blgp:1
	s_nop 0
	v_exp_f32_e32 v114, v114
	v_exp_f32_e32 v115, v115
	v_exp_f32_e32 v116, v116
	v_exp_f32_e32 v117, v117
	v_exp_f32_e32 v118, v118
	v_exp_f32_e32 v119, v119
	v_add_u32_e32 v173, s64, v200
	ds_read_b128 v[74:77], v173 offset:512
	ds_read_b128 v[78:81], v173 offset:1536
	s_waitcnt lgkmcnt(2)
	v_mfma_scale_f32_32x32x64_f8f6f4 v[18:33], v[66:73], v[146:153], v[18:33], v209, v209 op_sel_hi:[0,0,0] blgp:1
	v_exp_f32_e32 v120, v120
	v_exp_f32_e32 v121, v121
	v_exp_f32_e32 v122, v122
	v_exp_f32_e32 v123, v123
	v_exp_f32_e32 v124, v124
	v_exp_f32_e32 v125, v125
	ds_read_b128 v[66:69], v173
	ds_read_b128 v[70:73], v173 offset:1024
	v_mfma_scale_f32_32x32x64_f8f6f4 v[34:49], v[210:217], v[146:153], v[34:49], v209, v209 op_sel_hi:[0,0,0] blgp:1
	v_exp_f32_e32 v126, v126
	v_exp_f32_e32 v127, v127
	v_exp_f32_e32 v128, v128
	v_exp_f32_e32 v129, v129
	v_exp_f32_e32 v98, v98
	v_exp_f32_e32 v99, v99
	v_exp_f32_e32 v100, v100
	v_cvt_pk_bf8_f32 v146, v114, v115
	v_cvt_pk_bf8_f32 v147, v118, v119
	v_exp_f32_e32 v101, v101
	v_exp_f32_e32 v102, v102
	v_exp_f32_e32 v103, v103
	s_waitcnt lgkmcnt(0)
	v_mfma_scale_f32_32x32x64_f8f6f4 v[82:97], v[66:73], v[138:145], v[2:17], v209, v208 op_sel_hi:[0,0,0]
	global_load_lds_dwordx4 v[162:163], off
	ds_read_b128 v[164:167], v173 offset:4096
	ds_read_b128 v[168:171], v173 offset:5120
	v_cvt_pk_bf8_f32 v146, v116, v117 op_sel:[0,0,1]
	v_cvt_pk_bf8_f32 v147, v120, v121 op_sel:[0,0,1]
	v_cvt_pk_bf8_f32 v148, v122, v123
	v_cvt_pk_bf8_f32 v149, v126, v127
	ds_read_b128 v[114:117], v173 offset:4608
	ds_read_b128 v[118:121], v173 offset:5632
	v_exp_f32_e32 v104, v104
	v_exp_f32_e32 v105, v105
	s_waitcnt lgkmcnt(4)
	v_mfma_scale_f32_32x32x64_f8f6f4 v[66:81], v[74:81], v[138:145], v[2:17], v209, v208 op_sel_hi:[0,0,0]
	global_load_lds_dwordx4 v[162:163], off offset:1024
	v_cvt_pk_bf8_f32 v148, v124, v125 op_sel:[0,0,1]
	v_cvt_pk_bf8_f32 v149, v128, v129 op_sel:[0,0,1]
	ds_read_b128 v[122:125], v172 offset:20480
	ds_read_b128 v[126:129], v172 offset:21504
	v_exp_f32_e32 v106, v106
	v_exp_f32_e32 v107, v107
	v_exp_f32_e32 v108, v108
	s_waitcnt lgkmcnt(4)
	v_mfma_scale_f32_32x32x64_f8f6f4 v[82:97], v[164:171], v[130:137], v[82:97], v209, v208 op_sel_hi:[0,0,0]
	global_load_lds_dwordx4 v[162:163], off offset:2048
	s_mov_b32 m0, s3
	v_exp_f32_e32 v109, v109
	v_exp_f32_e32 v110, v110
	v_exp_f32_e32 v111, v111
	v_exp_f32_e32 v112, v112
	v_exp_f32_e32 v113, v113
	s_waitcnt lgkmcnt(2)
	v_mfma_scale_f32_32x32x64_f8f6f4 v[66:81], v[114:121], v[130:137], v[66:81], v209, v208 op_sel_hi:[0,0,0]
	v_cvt_pk_bf8_f32 v150, v98, v99
	v_cvt_pk_bf8_f32 v151, v102, v103
	v_cvt_pk_bf8_f32 v150, v100, v101 op_sel:[0,0,1]
	v_cvt_pk_bf8_f32 v151, v104, v105 op_sel:[0,0,1]
	v_cvt_pk_bf8_f32 v152, v106, v107
	v_cvt_pk_bf8_f32 v153, v110, v111
	v_cvt_pk_bf8_f32 v152, v108, v109 op_sel:[0,0,1]
	v_cvt_pk_bf8_f32 v153, v112, v113 op_sel:[0,0,1]
	ds_read_b128 v[98:101], v172 offset:20992
	ds_read_b128 v[102:105], v172 offset:22016
	s_waitcnt lgkmcnt(2)
	v_mfma_scale_f32_32x32x64_f8f6f4 v[50:65], v[122:129], v[146:153], v[50:65], v209, v209 op_sel_hi:[0,0,0] blgp:1
	s_nop 0
	v_exp_f32_e32 v82, v82
	v_exp_f32_e32 v83, v83
	v_exp_f32_e32 v84, v84
	v_exp_f32_e32 v85, v85
	v_exp_f32_e32 v86, v86
	v_exp_f32_e32 v87, v87
	s_waitcnt lgkmcnt(0)
	v_mfma_scale_f32_32x32x64_f8f6f4 v[18:33], v[98:105], v[146:153], v[18:33], v209, v209 op_sel_hi:[0,0,0] blgp:1
	v_exp_f32_e32 v88, v88
	v_exp_f32_e32 v89, v89
	v_exp_f32_e32 v90, v90
	v_exp_f32_e32 v91, v91
	v_exp_f32_e32 v92, v92
	v_exp_f32_e32 v93, v93
	v_mfma_scale_f32_32x32x64_f8f6f4 v[34:49], v[210:217], v[146:153], v[34:49], v209, v209 op_sel_hi:[0,0,0] blgp:1
	v_exp_f32_e32 v94, v94
	v_exp_f32_e32 v95, v95
	v_exp_f32_e32 v96, v96
	v_exp_f32_e32 v97, v97
	v_exp_f32_e32 v66, v66
	v_exp_f32_e32 v67, v67
	v_exp_f32_e32 v68, v68
	s_mov_b64 s[20:21], 0x6000
	s_cmpk_lg_i32 s61, 0x80
	v_lshl_add_u64 v[162:163], v[162:163], 0, s[20:21]
	s_cbranch_scc0 .LBB0_835
